# baseline (speedup 1.0000x reference)
.LBB2_356:
	ds_read_b128 v[140:143], v138
	ds_read_b128 v[154:157], v138 offset:1024
	ds_read_b128 v[158:161], v138 offset:2048
	ds_read_b128 v[164:167], v138 offset:3072
	s_lshl_b32 vcc_hi, s57, 7
	s_add_u32 s58, s88, vcc_hi
	s_addc_u32 s59, s89, 0
	s_add_u32 s82, s58, 0x80
	s_addc_u32 s83, s59, 0
	s_add_i32 s59, s97, 0xc000
	s_mov_b32 m0, s59
	s_add_i32 s58, s97, 0xe000
	ds_read_b128 v[168:171], v134
	ds_read_b128 v[172:175], v134 offset:1024
	ds_read_b128 v[176:179], v133
	ds_read_b128 v[184:187], v133 offset:1024
	ds_read_b128 v[188:191], v131
	ds_read_b128 v[192:195], v131 offset:1024
	ds_read_b128 v[196:199], v130
	ds_read_b128 v[200:203], v130 offset:1024
	global_load_lds_dwordx4 v162, s[82:83]
	s_mov_b32 m0, s58
	s_add_u32 s82, s82, 0x20000
	s_addc_u32 s83, s83, 0
	global_load_lds_dwordx4 v162, s[82:83]
	s_waitcnt lgkmcnt(8)
	s_barrier
	s_waitcnt lgkmcnt(7)
	v_mfma_f32_16x16x32_f16 v[102:105], v[140:143], v[168:171], v[102:105]
	v_mfma_f32_16x16x32_f16 v[98:101], v[158:161], v[168:171], v[98:101]
	s_waitcnt lgkmcnt(5)
	v_mfma_f32_16x16x32_f16 v[126:129], v[140:143], v[176:179], v[126:129]
	v_mfma_f32_16x16x32_f16 v[122:125], v[158:161], v[176:179], v[122:125]
	s_waitcnt lgkmcnt(3)
	v_mfma_f32_16x16x32_f16 v[118:121], v[140:143], v[188:191], v[118:121]
	v_mfma_f32_16x16x32_f16 v[114:117], v[158:161], v[188:191], v[114:117]
	s_waitcnt lgkmcnt(1)
	v_mfma_f32_16x16x32_f16 v[110:113], v[140:143], v[196:199], v[110:113]
	v_mfma_f32_16x16x32_f16 v[106:109], v[158:161], v[196:199], v[106:109]
	v_mfma_f32_16x16x32_f16 v[102:105], v[154:157], v[172:175], v[102:105]
	v_mfma_f32_16x16x32_f16 v[98:101], v[164:167], v[172:175], v[98:101]
	v_mfma_f32_16x16x32_f16 v[126:129], v[154:157], v[184:187], v[126:129]
	v_mfma_f32_16x16x32_f16 v[122:125], v[164:167], v[184:187], v[122:125]
	v_mfma_f32_16x16x32_f16 v[118:121], v[154:157], v[192:195], v[118:121]
	v_mfma_f32_16x16x32_f16 v[114:117], v[164:167], v[192:195], v[114:117]
	s_waitcnt lgkmcnt(0)
	v_mfma_f32_16x16x32_f16 v[110:113], v[154:157], v[200:203], v[110:113]
	v_mfma_f32_16x16x32_f16 v[106:109], v[164:167], v[200:203], v[106:109]
	s_barrier
	s_add_i32 vcc_lo, s57, 2
	s_lshl_b32 s78, vcc_lo, 7
	s_add_u32 s82, s92, s78
	s_addc_u32 s83, s93, 0
	s_mov_b32 m0, s84
	ds_read_b128 v[204:207], v137
	ds_read_b128 v[208:211], v137 offset:1024
	ds_read_b128 v[212:215], v137 offset:2048
	ds_read_b128 v[216:219], v137 offset:3072
	global_load_lds_dwordx4 v162, s[82:83]
	s_mov_b32 m0, s94
	s_add_u32 s82, s82, 0x20000
	s_addc_u32 s83, s83, 0
	global_load_lds_dwordx4 v162, s[82:83]
	s_barrier
	s_waitcnt lgkmcnt(0)
	v_mfma_f32_16x16x32_f16 v[94:97], v[204:207], v[168:171], v[94:97]
	v_mfma_f32_16x16x32_f16 v[90:93], v[212:215], v[168:171], v[90:93]
	v_mfma_f32_16x16x32_f16 v[86:89], v[204:207], v[176:179], v[86:89]
	v_mfma_f32_16x16x32_f16 v[82:85], v[212:215], v[176:179], v[82:85]
	v_mfma_f32_16x16x32_f16 v[78:81], v[204:207], v[188:191], v[78:81]
	v_mfma_f32_16x16x32_f16 v[74:77], v[212:215], v[188:191], v[74:77]
	v_mfma_f32_16x16x32_f16 v[70:73], v[204:207], v[196:199], v[70:73]
	v_mfma_f32_16x16x32_f16 v[66:69], v[212:215], v[196:199], v[66:69]
	v_mfma_f32_16x16x32_f16 v[94:97], v[208:211], v[172:175], v[94:97]
	v_mfma_f32_16x16x32_f16 v[90:93], v[216:219], v[172:175], v[90:93]
	v_mfma_f32_16x16x32_f16 v[86:89], v[208:211], v[184:187], v[86:89]
	v_mfma_f32_16x16x32_f16 v[82:85], v[216:219], v[184:187], v[82:85]
	v_mfma_f32_16x16x32_f16 v[78:81], v[208:211], v[192:195], v[78:81]
	v_mfma_f32_16x16x32_f16 v[74:77], v[216:219], v[192:195], v[74:77]
	v_mfma_f32_16x16x32_f16 v[70:73], v[208:211], v[200:203], v[70:73]
	v_mfma_f32_16x16x32_f16 v[66:69], v[216:219], v[200:203], v[66:69]
	s_add_u32 s82, s90, s78
	s_addc_u32 s83, s91, 0
	s_mov_b32 m0, s97
	s_barrier
	ds_read_b128 v[168:171], v134 offset:16384
	ds_read_b128 v[172:175], v134 offset:17408
	ds_read_b128 v[176:179], v133 offset:16384
	ds_read_b128 v[184:187], v133 offset:17408
	ds_read_b128 v[188:191], v131 offset:16384
	ds_read_b128 v[192:195], v131 offset:17408
	ds_read_b128 v[196:199], v130 offset:16384
	ds_read_b128 v[200:203], v130 offset:17408
	global_load_lds_dwordx4 v162, s[82:83]
	s_mov_b32 m0, s99
	s_add_u32 s82, s82, 0x20000
	s_addc_u32 s83, s83, 0
	global_load_lds_dwordx4 v162, s[82:83]
	s_barrier
	s_waitcnt lgkmcnt(7)
	v_mfma_f32_16x16x32_f16 v[62:65], v[140:143], v[168:171], v[62:65]
	v_mfma_f32_16x16x32_f16 v[58:61], v[158:161], v[168:171], v[58:61]
	s_waitcnt lgkmcnt(5)
	v_mfma_f32_16x16x32_f16 v[54:57], v[140:143], v[176:179], v[54:57]
	v_mfma_f32_16x16x32_f16 v[50:53], v[158:161], v[176:179], v[50:53]
	s_waitcnt lgkmcnt(3)
	v_mfma_f32_16x16x32_f16 v[46:49], v[140:143], v[188:191], v[46:49]
	v_mfma_f32_16x16x32_f16 v[42:45], v[158:161], v[188:191], v[42:45]
	s_waitcnt lgkmcnt(1)
	v_mfma_f32_16x16x32_f16 v[38:41], v[140:143], v[196:199], v[38:41]
	v_mfma_f32_16x16x32_f16 v[30:33], v[158:161], v[196:199], v[30:33]
	v_mfma_f32_16x16x32_f16 v[62:65], v[154:157], v[172:175], v[62:65]
	v_mfma_f32_16x16x32_f16 v[58:61], v[164:167], v[172:175], v[58:61]
	v_mfma_f32_16x16x32_f16 v[54:57], v[154:157], v[184:187], v[54:57]
	v_mfma_f32_16x16x32_f16 v[50:53], v[164:167], v[184:187], v[50:53]
	v_mfma_f32_16x16x32_f16 v[46:49], v[154:157], v[192:195], v[46:49]
	v_mfma_f32_16x16x32_f16 v[42:45], v[164:167], v[192:195], v[42:45]
	s_waitcnt lgkmcnt(0)
	v_mfma_f32_16x16x32_f16 v[38:41], v[154:157], v[200:203], v[38:41]
	v_mfma_f32_16x16x32_f16 v[30:33], v[164:167], v[200:203], v[30:33]
	s_barrier
	s_add_u32 s82, s34, s78
	s_addc_u32 s83, s35, 0
	s_mov_b32 m0, s95
	s_nop 0
	global_load_lds_dwordx4 v162, s[82:83]
	s_mov_b32 m0, s33
	s_add_u32 s82, s82, 0x20000
	s_addc_u32 s83, s83, 0
	global_load_lds_dwordx4 v162, s[82:83]
	s_waitcnt vmcnt(6)
	s_barrier
	v_mfma_f32_16x16x32_f16 v[34:37], v[204:207], v[168:171], v[34:37]
	v_mfma_f32_16x16x32_f16 v[26:29], v[212:215], v[168:171], v[26:29]
	v_mfma_f32_16x16x32_f16 v[22:25], v[204:207], v[176:179], v[22:25]
	v_mfma_f32_16x16x32_f16 v[18:21], v[212:215], v[176:179], v[18:21]
	v_mfma_f32_16x16x32_f16 v[14:17], v[204:207], v[188:191], v[14:17]
	v_mfma_f32_16x16x32_f16 v[10:13], v[212:215], v[188:191], v[10:13]
	v_mfma_f32_16x16x32_f16 v[6:9], v[204:207], v[196:199], v[6:9]
	v_mfma_f32_16x16x32_f16 v[2:5], v[212:215], v[196:199], v[2:5]
	v_mfma_f32_16x16x32_f16 v[34:37], v[208:211], v[172:175], v[34:37]
	v_mfma_f32_16x16x32_f16 v[26:29], v[216:219], v[172:175], v[26:29]
	v_mfma_f32_16x16x32_f16 v[22:25], v[208:211], v[184:187], v[22:25]
	v_mfma_f32_16x16x32_f16 v[18:21], v[216:219], v[184:187], v[18:21]
	v_mfma_f32_16x16x32_f16 v[14:17], v[208:211], v[192:195], v[14:17]
	v_mfma_f32_16x16x32_f16 v[10:13], v[216:219], v[192:195], v[10:13]
	v_mfma_f32_16x16x32_f16 v[6:9], v[208:211], v[200:203], v[6:9]
	v_mfma_f32_16x16x32_f16 v[2:5], v[216:219], v[200:203], v[2:5]
	s_barrier
	ds_read_b128 v[140:143], v136
	ds_read_b128 v[154:157], v136 offset:1024
	ds_read_b128 v[158:161], v136 offset:2048
	ds_read_b128 v[164:167], v136 offset:3072
	s_add_u32 s82, s88, s78
	s_addc_u32 s83, s89, 0
	s_mov_b32 m0, s11
	ds_read_b128 v[168:171], v134 offset:32768
	ds_read_b128 v[172:175], v134 offset:33792
	ds_read_b128 v[176:179], v133 offset:32768
	ds_read_b128 v[184:187], v133 offset:33792
	ds_read_b128 v[188:191], v131 offset:32768
	ds_read_b128 v[192:195], v131 offset:33792
	ds_read_b128 v[196:199], v130 offset:32768
	ds_read_b128 v[200:203], v130 offset:33792
	global_load_lds_dwordx4 v162, s[82:83]
	s_mov_b32 m0, s56
	s_add_u32 s82, s82, 0x20000
	s_addc_u32 s83, s83, 0
	global_load_lds_dwordx4 v162, s[82:83]
	s_waitcnt lgkmcnt(8)
	s_barrier
	s_waitcnt lgkmcnt(7)
	v_mfma_f32_16x16x32_f16 v[102:105], v[140:143], v[168:171], v[102:105]
	v_mfma_f32_16x16x32_f16 v[98:101], v[158:161], v[168:171], v[98:101]
	s_waitcnt lgkmcnt(5)
	v_mfma_f32_16x16x32_f16 v[126:129], v[140:143], v[176:179], v[126:129]
	v_mfma_f32_16x16x32_f16 v[122:125], v[158:161], v[176:179], v[122:125]
	s_waitcnt lgkmcnt(3)
	v_mfma_f32_16x16x32_f16 v[118:121], v[140:143], v[188:191], v[118:121]
	v_mfma_f32_16x16x32_f16 v[114:117], v[158:161], v[188:191], v[114:117]
	s_waitcnt lgkmcnt(1)
	v_mfma_f32_16x16x32_f16 v[110:113], v[140:143], v[196:199], v[110:113]
	v_mfma_f32_16x16x32_f16 v[106:109], v[158:161], v[196:199], v[106:109]
	v_mfma_f32_16x16x32_f16 v[102:105], v[154:157], v[172:175], v[102:105]
	v_mfma_f32_16x16x32_f16 v[98:101], v[164:167], v[172:175], v[98:101]
	v_mfma_f32_16x16x32_f16 v[126:129], v[154:157], v[184:187], v[126:129]
	v_mfma_f32_16x16x32_f16 v[122:125], v[164:167], v[184:187], v[122:125]
	v_mfma_f32_16x16x32_f16 v[118:121], v[154:157], v[192:195], v[118:121]
	v_mfma_f32_16x16x32_f16 v[114:117], v[164:167], v[192:195], v[114:117]
	s_waitcnt lgkmcnt(0)
	v_mfma_f32_16x16x32_f16 v[110:113], v[154:157], v[200:203], v[110:113]
	v_mfma_f32_16x16x32_f16 v[106:109], v[164:167], v[200:203], v[106:109]
	s_barrier
	s_add_u32 s78, s92, vcc_hi
	s_addc_u32 s79, s93, 0
	s_add_u32 s82, s78, 0x180
	s_addc_u32 s83, s79, 0
	s_add_i32 m0, s97, 0x18000
	ds_read_b128 v[204:207], v135
	ds_read_b128 v[208:211], v135 offset:1024
	ds_read_b128 v[212:215], v135 offset:2048
	ds_read_b128 v[216:219], v135 offset:3072
	global_load_lds_dwordx4 v162, s[82:83]
	s_add_i32 m0, s97, 0x1a000
	s_add_u32 s82, s82, 0x20000
	s_addc_u32 s83, s83, 0
	global_load_lds_dwordx4 v162, s[82:83]
	s_barrier
	s_waitcnt lgkmcnt(0)
	v_mfma_f32_16x16x32_f16 v[94:97], v[204:207], v[168:171], v[94:97]
	v_mfma_f32_16x16x32_f16 v[90:93], v[212:215], v[168:171], v[90:93]
	v_mfma_f32_16x16x32_f16 v[86:89], v[204:207], v[176:179], v[86:89]
	v_mfma_f32_16x16x32_f16 v[82:85], v[212:215], v[176:179], v[82:85]
	v_mfma_f32_16x16x32_f16 v[78:81], v[204:207], v[188:191], v[78:81]
	v_mfma_f32_16x16x32_f16 v[74:77], v[212:215], v[188:191], v[74:77]
	v_mfma_f32_16x16x32_f16 v[70:73], v[204:207], v[196:199], v[70:73]
	v_mfma_f32_16x16x32_f16 v[66:69], v[212:215], v[196:199], v[66:69]
	v_mfma_f32_16x16x32_f16 v[94:97], v[208:211], v[172:175], v[94:97]
	v_mfma_f32_16x16x32_f16 v[90:93], v[216:219], v[172:175], v[90:93]
	v_mfma_f32_16x16x32_f16 v[86:89], v[208:211], v[184:187], v[86:89]
	v_mfma_f32_16x16x32_f16 v[82:85], v[216:219], v[184:187], v[82:85]
	v_mfma_f32_16x16x32_f16 v[78:81], v[208:211], v[192:195], v[78:81]
	v_mfma_f32_16x16x32_f16 v[74:77], v[216:219], v[192:195], v[74:77]
	v_mfma_f32_16x16x32_f16 v[70:73], v[208:211], v[200:203], v[70:73]
	v_mfma_f32_16x16x32_f16 v[66:69], v[216:219], v[200:203], v[66:69]
	s_add_u32 s78, s90, vcc_hi
	s_addc_u32 s79, s91, 0
	s_add_u32 s82, s78, 0x180
	s_addc_u32 s83, s79, 0
	s_mov_b32 m0, s52
	s_barrier
	ds_read_b128 v[168:171], v134 offset:49152
	ds_read_b128 v[172:175], v134 offset:50176
	ds_read_b128 v[176:179], v133 offset:49152
	ds_read_b128 v[184:187], v133 offset:50176
	ds_read_b128 v[188:191], v131 offset:49152
	ds_read_b128 v[192:195], v131 offset:50176
	ds_read_b128 v[196:199], v130 offset:49152
	ds_read_b128 v[200:203], v130 offset:50176
	global_load_lds_dwordx4 v162, s[82:83]
	s_mov_b32 m0, s53
	s_add_u32 s82, s82, 0x20000
	s_addc_u32 s83, s83, 0
	global_load_lds_dwordx4 v162, s[82:83]
	s_barrier
	s_waitcnt lgkmcnt(7)
	v_mfma_f32_16x16x32_f16 v[62:65], v[140:143], v[168:171], v[62:65]
	v_mfma_f32_16x16x32_f16 v[58:61], v[158:161], v[168:171], v[58:61]
	s_waitcnt lgkmcnt(5)
	v_mfma_f32_16x16x32_f16 v[54:57], v[140:143], v[176:179], v[54:57]
	v_mfma_f32_16x16x32_f16 v[50:53], v[158:161], v[176:179], v[50:53]
	s_waitcnt lgkmcnt(3)
	v_mfma_f32_16x16x32_f16 v[46:49], v[140:143], v[188:191], v[46:49]
	v_mfma_f32_16x16x32_f16 v[42:45], v[158:161], v[188:191], v[42:45]
	s_waitcnt lgkmcnt(1)
	v_mfma_f32_16x16x32_f16 v[38:41], v[140:143], v[196:199], v[38:41]
	v_mfma_f32_16x16x32_f16 v[30:33], v[158:161], v[196:199], v[30:33]
	v_mfma_f32_16x16x32_f16 v[62:65], v[154:157], v[172:175], v[62:65]
	v_mfma_f32_16x16x32_f16 v[58:61], v[164:167], v[172:175], v[58:61]
	v_mfma_f32_16x16x32_f16 v[54:57], v[154:157], v[184:187], v[54:57]
	v_mfma_f32_16x16x32_f16 v[50:53], v[164:167], v[184:187], v[50:53]
	v_mfma_f32_16x16x32_f16 v[46:49], v[154:157], v[192:195], v[46:49]
	v_mfma_f32_16x16x32_f16 v[42:45], v[164:167], v[192:195], v[42:45]
	s_waitcnt lgkmcnt(0)
	v_mfma_f32_16x16x32_f16 v[38:41], v[154:157], v[200:203], v[38:41]
	v_mfma_f32_16x16x32_f16 v[30:33], v[164:167], v[200:203], v[30:33]
	s_barrier
	s_add_u32 s78, s34, vcc_hi
	s_addc_u32 s79, s35, 0
	s_add_u32 s82, s78, 0x180
	s_addc_u32 s83, s79, 0
	s_add_i32 m0, s97, 0x1c000
	s_nop 0
	global_load_lds_dwordx4 v162, s[82:83]
	s_add_i32 m0, s97, 0x1e000
	s_add_u32 s82, s82, 0x20000
	s_addc_u32 s83, s83, 0
	global_load_lds_dwordx4 v162, s[82:83]
	s_waitcnt vmcnt(6)
	s_barrier
	v_mfma_f32_16x16x32_f16 v[34:37], v[204:207], v[168:171], v[34:37]
	v_mfma_f32_16x16x32_f16 v[26:29], v[212:215], v[168:171], v[26:29]
	v_mfma_f32_16x16x32_f16 v[22:25], v[204:207], v[176:179], v[22:25]
	v_mfma_f32_16x16x32_f16 v[18:21], v[212:215], v[176:179], v[18:21]
	v_mfma_f32_16x16x32_f16 v[14:17], v[204:207], v[188:191], v[14:17]
	v_mfma_f32_16x16x32_f16 v[10:13], v[212:215], v[188:191], v[10:13]
	v_mfma_f32_16x16x32_f16 v[6:9], v[204:207], v[196:199], v[6:9]
	v_mfma_f32_16x16x32_f16 v[2:5], v[212:215], v[196:199], v[2:5]
	v_mfma_f32_16x16x32_f16 v[34:37], v[208:211], v[172:175], v[34:37]
	v_mfma_f32_16x16x32_f16 v[26:29], v[216:219], v[172:175], v[26:29]
	v_mfma_f32_16x16x32_f16 v[22:25], v[208:211], v[184:187], v[22:25]
	v_mfma_f32_16x16x32_f16 v[18:21], v[216:219], v[184:187], v[18:21]
	v_mfma_f32_16x16x32_f16 v[14:17], v[208:211], v[192:195], v[14:17]
	v_mfma_f32_16x16x32_f16 v[10:13], v[216:219], v[192:195], v[10:13]
	v_mfma_f32_16x16x32_f16 v[6:9], v[208:211], v[200:203], v[6:9]
	v_mfma_f32_16x16x32_f16 v[2:5], v[216:219], v[200:203], v[2:5]
	s_cmp_lt_u32 s57, 12
	s_mov_b32 s57, vcc_lo
	s_barrier
	s_cbranch_scc1 .LBB2_356
	s_add_u32 s34, s88, 0x780
	s_addc_u32 s35, s89, 0
	ds_read_b128 v[140:143], v138
	ds_read_b128 v[154:157], v138 offset:1024
	ds_read_b128 v[158:161], v138 offset:2048
	ds_read_b128 v[164:167], v138 offset:3072
	ds_read_b128 v[168:171], v134
	ds_read_b128 v[172:175], v134 offset:1024
	ds_read_b128 v[176:179], v133
	ds_read_b128 v[184:187], v133 offset:1024
	ds_read_b128 v[188:191], v131
	ds_read_b128 v[192:195], v131 offset:1024
	ds_read_b128 v[196:199], v130
	ds_read_b128 v[200:203], v130 offset:1024
	v_lshl_add_u64 v[138:139], s[34:35], 0, v[162:163]
	s_add_u32 s34, s34, 0x20000
	s_mov_b32 m0, s59
	s_addc_u32 s35, s35, 0
	global_load_lds_dwordx4 v[138:139], off
	s_mov_b32 m0, s58
	v_lshl_add_u64 v[138:139], s[34:35], 0, v[162:163]
	global_load_lds_dwordx4 v[138:139], off
	s_barrier
	s_waitcnt lgkmcnt(0)
	v_mfma_f32_16x16x32_f16 v[102:105], v[140:143], v[168:171], v[102:105]
	v_mfma_f32_16x16x32_f16 v[98:101], v[158:161], v[168:171], v[98:101]
	v_mfma_f32_16x16x32_f16 v[126:129], v[140:143], v[176:179], v[126:129]
	v_mfma_f32_16x16x32_f16 v[122:125], v[158:161], v[176:179], v[122:125]
	v_mfma_f32_16x16x32_f16 v[118:121], v[140:143], v[188:191], v[118:121]
	v_mfma_f32_16x16x32_f16 v[114:117], v[158:161], v[188:191], v[114:117]
	v_mfma_f32_16x16x32_f16 v[110:113], v[140:143], v[196:199], v[110:113]
	v_mfma_f32_16x16x32_f16 v[106:109], v[158:161], v[196:199], v[106:109]
	v_mfma_f32_16x16x32_f16 v[102:105], v[154:157], v[172:175], v[102:105]
	v_mfma_f32_16x16x32_f16 v[98:101], v[164:167], v[172:175], v[98:101]
	v_mfma_f32_16x16x32_f16 v[126:129], v[154:157], v[184:187], v[126:129]
	v_mfma_f32_16x16x32_f16 v[122:125], v[164:167], v[184:187], v[122:125]
	v_mfma_f32_16x16x32_f16 v[118:121], v[154:157], v[192:195], v[118:121]
	v_mfma_f32_16x16x32_f16 v[114:117], v[164:167], v[192:195], v[114:117]
	v_mfma_f32_16x16x32_f16 v[110:113], v[154:157], v[200:203], v[110:113]
	v_mfma_f32_16x16x32_f16 v[106:109], v[164:167], v[200:203], v[106:109]
	s_barrier
	ds_read_b128 v[204:207], v137
	ds_read_b128 v[208:211], v137 offset:1024
	ds_read_b128 v[212:215], v137 offset:2048
	ds_read_b128 v[216:219], v137 offset:3072
	s_barrier
	s_waitcnt lgkmcnt(0)
	v_mfma_f32_16x16x32_f16 v[94:97], v[204:207], v[168:171], v[94:97]
	v_mfma_f32_16x16x32_f16 v[94:97], v[208:211], v[172:175], v[94:97]
	v_mfma_f32_16x16x32_f16 v[90:93], v[212:215], v[168:171], v[90:93]
	v_mfma_f32_16x16x32_f16 v[86:89], v[204:207], v[176:179], v[86:89]
	v_mfma_f32_16x16x32_f16 v[82:85], v[212:215], v[176:179], v[82:85]
	v_mfma_f32_16x16x32_f16 v[78:81], v[204:207], v[188:191], v[78:81]
	v_mfma_f32_16x16x32_f16 v[74:77], v[212:215], v[188:191], v[74:77]
	v_mfma_f32_16x16x32_f16 v[70:73], v[204:207], v[196:199], v[70:73]
	v_mfma_f32_16x16x32_f16 v[66:69], v[212:215], v[196:199], v[66:69]
	v_mfma_f32_16x16x32_f16 v[168:171], v[216:219], v[172:175], v[90:93]
	v_mfma_f32_16x16x32_f16 v[172:175], v[208:211], v[184:187], v[86:89]
	v_mfma_f32_16x16x32_f16 v[176:179], v[216:219], v[184:187], v[82:85]
	v_mfma_f32_16x16x32_f16 v[184:187], v[208:211], v[192:195], v[78:81]
	v_mfma_f32_16x16x32_f16 v[188:191], v[216:219], v[192:195], v[74:77]
	v_mfma_f32_16x16x32_f16 v[192:195], v[208:211], v[200:203], v[70:73]
	v_mfma_f32_16x16x32_f16 v[196:199], v[216:219], v[200:203], v[66:69]
	s_barrier
	s_nop 0
	ds_read_b128 v[66:69], v134 offset:16384
	ds_read_b128 v[70:73], v134 offset:17408
	ds_read_b128 v[74:77], v133 offset:16384
	ds_read_b128 v[78:81], v133 offset:17408
	ds_read_b128 v[82:85], v131 offset:16384
	ds_read_b128 v[86:89], v131 offset:17408
	ds_read_b128 v[90:93], v130 offset:16384
	ds_read_b128 v[200:203], v130 offset:17408
	s_waitcnt vmcnt(4)
	s_barrier
	s_waitcnt lgkmcnt(0)
	v_mfma_f32_16x16x32_f16 v[62:65], v[140:143], v[66:69], v[62:65]
	v_mfma_f32_16x16x32_f16 v[58:61], v[158:161], v[66:69], v[58:61]
	v_mfma_f32_16x16x32_f16 v[54:57], v[140:143], v[74:77], v[54:57]
	v_mfma_f32_16x16x32_f16 v[50:53], v[158:161], v[74:77], v[50:53]
	v_mfma_f32_16x16x32_f16 v[46:49], v[140:143], v[82:85], v[46:49]
	v_mfma_f32_16x16x32_f16 v[42:45], v[158:161], v[82:85], v[42:45]
	v_mfma_f32_16x16x32_f16 v[38:41], v[140:143], v[90:93], v[38:41]
	v_mfma_f32_16x16x32_f16 v[62:65], v[154:157], v[70:73], v[62:65]
	v_mfma_f32_16x16x32_f16 v[58:61], v[164:167], v[70:73], v[58:61]
	v_mfma_f32_16x16x32_f16 v[54:57], v[154:157], v[78:81], v[54:57]
	v_mfma_f32_16x16x32_f16 v[50:53], v[164:167], v[78:81], v[50:53]
	v_mfma_f32_16x16x32_f16 v[46:49], v[154:157], v[86:89], v[46:49]
	v_mfma_f32_16x16x32_f16 v[42:45], v[164:167], v[86:89], v[42:45]
	v_mfma_f32_16x16x32_f16 v[38:41], v[154:157], v[200:203], v[38:41]
	v_mfma_f32_16x16x32_f16 v[30:33], v[158:161], v[90:93], v[30:33]
	v_mfma_f32_16x16x32_f16 v[138:141], v[164:167], v[200:203], v[30:33]
	v_mfma_f32_16x16x32_f16 v[30:33], v[204:207], v[66:69], v[34:37]
	v_mfma_f32_16x16x32_f16 v[34:37], v[208:211], v[70:73], v[30:33]
	v_mfma_f32_16x16x32_f16 v[26:29], v[212:215], v[66:69], v[26:29]
	v_mfma_f32_16x16x32_f16 v[22:25], v[204:207], v[74:77], v[22:25]
	v_mfma_f32_16x16x32_f16 v[18:21], v[212:215], v[74:77], v[18:21]
	v_mfma_f32_16x16x32_f16 v[14:17], v[204:207], v[82:85], v[14:17]
	v_mfma_f32_16x16x32_f16 v[10:13], v[212:215], v[82:85], v[10:13]
	v_mfma_f32_16x16x32_f16 v[6:9], v[204:207], v[90:93], v[6:9]
	v_mfma_f32_16x16x32_f16 v[2:5], v[212:215], v[90:93], v[2:5]
	v_mfma_f32_16x16x32_f16 v[142:145], v[216:219], v[70:73], v[26:29]
	v_mfma_f32_16x16x32_f16 v[154:157], v[208:211], v[78:81], v[22:25]
	v_mfma_f32_16x16x32_f16 v[158:161], v[216:219], v[78:81], v[18:21]
	v_mfma_f32_16x16x32_f16 v[164:167], v[208:211], v[86:89], v[14:17]
	v_mfma_f32_16x16x32_f16 v[220:223], v[216:219], v[86:89], v[10:13]
	v_mfma_f32_16x16x32_f16 v[204:207], v[208:211], v[200:203], v[6:9]
	v_mfma_f32_16x16x32_f16 v[200:203], v[216:219], v[200:203], v[2:5]
	s_barrier
	s_nop 0
	ds_read_b128 v[2:5], v136
	ds_read_b128 v[6:9], v136 offset:1024
	ds_read_b128 v[208:211], v136 offset:2048
	ds_read_b128 v[212:215], v136 offset:3072
	ds_read_b128 v[10:13], v134 offset:32768
	ds_read_b128 v[14:17], v134 offset:33792
	ds_read_b128 v[18:21], v133 offset:32768
	ds_read_b128 v[22:25], v133 offset:33792
	ds_read_b128 v[26:29], v131 offset:32768
	ds_read_b128 v[30:33], v131 offset:33792
	ds_read_b128 v[216:219], v130 offset:32768
	ds_read_b128 v[224:227], v130 offset:33792
	s_waitcnt vmcnt(2)
	s_barrier
	s_waitcnt lgkmcnt(0)
	v_mfma_f32_16x16x32_f16 v[66:69], v[2:5], v[10:13], v[102:105]
	v_mfma_f32_16x16x32_f16 v[90:93], v[6:9], v[14:17], v[66:69]
	v_mfma_f32_16x16x32_f16 v[66:69], v[208:211], v[10:13], v[98:101]
	v_mfma_f32_16x16x32_f16 v[98:101], v[212:215], v[14:17], v[66:69]
	v_mfma_f32_16x16x32_f16 v[66:69], v[2:5], v[18:21], v[126:129]
	v_mfma_f32_16x16x32_f16 v[82:85], v[6:9], v[22:25], v[66:69]
	v_mfma_f32_16x16x32_f16 v[66:69], v[208:211], v[18:21], v[122:125]
	v_mfma_f32_16x16x32_f16 v[86:89], v[212:215], v[22:25], v[66:69]
	v_mfma_f32_16x16x32_f16 v[66:69], v[2:5], v[26:29], v[118:121]
	v_mfma_f32_16x16x32_f16 v[74:77], v[6:9], v[30:33], v[66:69]
	v_mfma_f32_16x16x32_f16 v[66:69], v[208:211], v[26:29], v[114:117]
	v_mfma_f32_16x16x32_f16 v[78:81], v[212:215], v[30:33], v[66:69]
	v_mfma_f32_16x16x32_f16 v[66:69], v[2:5], v[216:219], v[110:113]
	v_mfma_f32_16x16x32_f16 v[70:73], v[208:211], v[216:219], v[106:109]
	v_mfma_f32_16x16x32_f16 v[66:69], v[6:9], v[224:227], v[66:69]
	v_mfma_f32_16x16x32_f16 v[70:73], v[212:215], v[224:227], v[70:73]
	s_barrier
	ds_read_b128 v[228:231], v135
	ds_read_b128 v[232:235], v135 offset:1024
	ds_read_b128 v[236:239], v135 offset:2048
	ds_read_b128 v[240:243], v135 offset:3072
	s_waitcnt vmcnt(0)
	s_barrier
	s_waitcnt lgkmcnt(0)
	v_mfma_f32_16x16x32_f16 v[94:97], v[228:231], v[10:13], v[94:97]
	v_mfma_f32_16x16x32_f16 v[10:13], v[236:239], v[10:13], v[168:171]
	v_mfma_f32_16x16x32_f16 v[126:129], v[240:243], v[14:17], v[10:13]
	v_mfma_f32_16x16x32_f16 v[10:13], v[228:231], v[18:21], v[172:175]
	v_mfma_f32_16x16x32_f16 v[114:117], v[232:235], v[22:25], v[10:13]
	v_mfma_f32_16x16x32_f16 v[10:13], v[236:239], v[18:21], v[176:179]
	v_mfma_f32_16x16x32_f16 v[118:121], v[240:243], v[22:25], v[10:13]
	v_mfma_f32_16x16x32_f16 v[10:13], v[228:231], v[26:29], v[184:187]
	v_mfma_f32_16x16x32_f16 v[106:109], v[232:235], v[30:33], v[10:13]
	v_mfma_f32_16x16x32_f16 v[10:13], v[236:239], v[26:29], v[188:191]
	v_mfma_f32_16x16x32_f16 v[110:113], v[240:243], v[30:33], v[10:13]
	v_mfma_f32_16x16x32_f16 v[10:13], v[228:231], v[216:219], v[192:195]
	v_mfma_f32_16x16x32_f16 v[122:125], v[232:235], v[14:17], v[94:97]
	v_mfma_f32_16x16x32_f16 v[94:97], v[232:235], v[224:227], v[10:13]
	v_mfma_f32_16x16x32_f16 v[10:13], v[236:239], v[216:219], v[196:199]
	v_mfma_f32_16x16x32_f16 v[102:105], v[240:243], v[224:227], v[10:13]
	s_barrier
	ds_read_b128 v[168:171], v134 offset:49152
	ds_read_b128 v[134:137], v134 offset:50176
	ds_read_b128 v[172:175], v133 offset:49152
	ds_read_b128 v[176:179], v133 offset:50176
	ds_read_b128 v[184:187], v131 offset:49152
	ds_read_b128 v[188:191], v131 offset:50176
	ds_read_b128 v[192:195], v130 offset:49152
	ds_read_b128 v[196:199], v130 offset:50176
	s_barrier
	s_waitcnt lgkmcnt(0)
	v_mfma_f32_16x16x32_f16 v[10:13], v[2:5], v[168:171], v[62:65]
	v_mfma_f32_16x16x32_f16 v[26:29], v[6:9], v[134:137], v[10:13]
	v_mfma_f32_16x16x32_f16 v[10:13], v[208:211], v[168:171], v[58:61]
	v_mfma_f32_16x16x32_f16 v[30:33], v[212:215], v[134:137], v[10:13]
	v_mfma_f32_16x16x32_f16 v[10:13], v[2:5], v[172:175], v[54:57]
	v_mfma_f32_16x16x32_f16 v[18:21], v[6:9], v[176:179], v[10:13]
	v_mfma_f32_16x16x32_f16 v[10:13], v[208:211], v[172:175], v[50:53]
	v_mfma_f32_16x16x32_f16 v[22:25], v[212:215], v[176:179], v[10:13]
	v_mfma_f32_16x16x32_f16 v[10:13], v[2:5], v[184:187], v[46:49]
	v_mfma_f32_16x16x32_f16 v[2:5], v[2:5], v[192:195], v[38:41]
	v_mfma_f32_16x16x32_f16 v[10:13], v[6:9], v[188:191], v[10:13]
	v_mfma_f32_16x16x32_f16 v[14:17], v[208:211], v[184:187], v[42:45]
	v_mfma_f32_16x16x32_f16 v[2:5], v[6:9], v[196:199], v[2:5]
	v_mfma_f32_16x16x32_f16 v[6:9], v[208:211], v[192:195], v[138:141]
	v_mfma_f32_16x16x32_f16 v[14:17], v[212:215], v[188:191], v[14:17]
	v_mfma_f32_16x16x32_f16 v[6:9], v[212:215], v[196:199], v[6:9]
	v_mfma_f32_16x16x32_f16 v[34:37], v[228:231], v[168:171], v[34:37]
	v_mfma_f32_16x16x32_f16 v[58:61], v[232:235], v[134:137], v[34:37]
	v_mfma_f32_16x16x32_f16 v[34:37], v[236:239], v[168:171], v[142:145]
	v_mfma_f32_16x16x32_f16 v[62:65], v[240:243], v[134:137], v[34:37]
	v_mfma_f32_16x16x32_f16 v[34:37], v[228:231], v[172:175], v[154:157]
	v_mfma_f32_16x16x32_f16 v[50:53], v[232:235], v[176:179], v[34:37]
	v_mfma_f32_16x16x32_f16 v[34:37], v[236:239], v[172:175], v[158:161]
	v_mfma_f32_16x16x32_f16 v[54:57], v[240:243], v[176:179], v[34:37]
	v_mfma_f32_16x16x32_f16 v[34:37], v[228:231], v[184:187], v[164:167]
	v_mfma_f32_16x16x32_f16 v[42:45], v[232:235], v[188:191], v[34:37]
	v_mfma_f32_16x16x32_f16 v[34:37], v[236:239], v[184:187], v[220:223]
	v_mfma_f32_16x16x32_f16 v[46:49], v[240:243], v[188:191], v[34:37]
	v_mfma_f32_16x16x32_f16 v[34:37], v[228:231], v[192:195], v[204:207]
	v_mfma_f32_16x16x32_f16 v[38:41], v[236:239], v[192:195], v[200:203]
	v_mfma_f32_16x16x32_f16 v[34:37], v[232:235], v[196:199], v[34:37]
	v_mfma_f32_16x16x32_f16 v[38:41], v[240:243], v[196:199], v[38:41]

.LBB2_382:
	ds_read_b128 v[152:155], v151
	ds_read_b128 v[156:159], v151 offset:1024
	ds_read_b128 v[164:167], v151 offset:2048
	ds_read_b128 v[168:171], v151 offset:3072
	s_lshl_b32 s58, s84, 7
	s_add_u32 s59, s24, s58
	s_addc_u32 s91, s25, 0
	s_add_u32 s92, s59, 0x80
	s_addc_u32 s93, s91, 0
	s_add_i32 s56, s52, 0xc000
	s_mov_b32 m0, s56
	s_add_i32 s33, s52, 0xe000
	ds_read_b128 v[172:175], v147
	ds_read_b128 v[176:179], v147 offset:1024
	ds_read_b128 v[184:187], v146
	ds_read_b128 v[188:191], v146 offset:1024
	ds_read_b128 v[192:195], v145
	ds_read_b128 v[196:199], v145 offset:1024
	ds_read_b128 v[200:203], v144
	ds_read_b128 v[204:207], v144 offset:1024
	global_load_lds_dwordx4 v132, s[92:93]
	s_mov_b32 m0, s33
	s_nop 0
	global_load_lds_dwordx4 v130, s[92:93]
	s_waitcnt lgkmcnt(8)
	s_barrier
	s_waitcnt lgkmcnt(7)
	v_mfma_f32_16x16x32_f16 v[126:129], v[152:155], v[172:175], v[126:129]
	v_mfma_f32_16x16x32_f16 v[122:125], v[164:167], v[172:175], v[122:125]
	s_waitcnt lgkmcnt(5)
	v_mfma_f32_16x16x32_f16 v[118:121], v[152:155], v[184:187], v[118:121]
	v_mfma_f32_16x16x32_f16 v[114:117], v[164:167], v[184:187], v[114:117]
	s_waitcnt lgkmcnt(3)
	v_mfma_f32_16x16x32_f16 v[110:113], v[152:155], v[192:195], v[110:113]
	v_mfma_f32_16x16x32_f16 v[106:109], v[164:167], v[192:195], v[106:109]
	s_waitcnt lgkmcnt(1)
	v_mfma_f32_16x16x32_f16 v[102:105], v[152:155], v[200:203], v[102:105]
	v_mfma_f32_16x16x32_f16 v[98:101], v[164:167], v[200:203], v[98:101]
	v_mfma_f32_16x16x32_f16 v[126:129], v[156:159], v[176:179], v[126:129]
	v_mfma_f32_16x16x32_f16 v[122:125], v[168:171], v[176:179], v[122:125]
	v_mfma_f32_16x16x32_f16 v[118:121], v[156:159], v[188:191], v[118:121]
	v_mfma_f32_16x16x32_f16 v[114:117], v[168:171], v[188:191], v[114:117]
	v_mfma_f32_16x16x32_f16 v[110:113], v[156:159], v[196:199], v[110:113]
	v_mfma_f32_16x16x32_f16 v[106:109], v[168:171], v[196:199], v[106:109]
	s_waitcnt lgkmcnt(0)
	v_mfma_f32_16x16x32_f16 v[102:105], v[156:159], v[204:207], v[102:105]
	v_mfma_f32_16x16x32_f16 v[98:101], v[168:171], v[204:207], v[98:101]
	s_barrier
	s_add_i32 s57, s84, 2
	s_lshl_b32 s82, s57, 7
	s_add_u32 s92, s4, s82
	s_addc_u32 s93, s5, 0
	s_mov_b32 m0, s53
	ds_read_b128 v[208:211], v150
	ds_read_b128 v[212:215], v150 offset:1024
	ds_read_b128 v[216:219], v150 offset:2048
	ds_read_b128 v[220:223], v150 offset:3072
	global_load_lds_dwordx4 v162, s[92:93]
	s_mov_b32 m0, s55
	s_add_u32 s92, s92, 0x40000
	s_addc_u32 s93, s93, 0
	global_load_lds_dwordx4 v162, s[92:93]
	s_barrier
	s_waitcnt lgkmcnt(0)
	v_mfma_f32_16x16x32_f16 v[94:97], v[208:211], v[172:175], v[94:97]
	v_mfma_f32_16x16x32_f16 v[90:93], v[216:219], v[172:175], v[90:93]
	v_mfma_f32_16x16x32_f16 v[86:89], v[208:211], v[184:187], v[86:89]
	v_mfma_f32_16x16x32_f16 v[82:85], v[216:219], v[184:187], v[82:85]
	v_mfma_f32_16x16x32_f16 v[78:81], v[208:211], v[192:195], v[78:81]
	v_mfma_f32_16x16x32_f16 v[74:77], v[216:219], v[192:195], v[74:77]
	v_mfma_f32_16x16x32_f16 v[70:73], v[208:211], v[200:203], v[70:73]
	v_mfma_f32_16x16x32_f16 v[66:69], v[216:219], v[200:203], v[66:69]
	v_mfma_f32_16x16x32_f16 v[94:97], v[212:215], v[176:179], v[94:97]
	v_mfma_f32_16x16x32_f16 v[90:93], v[220:223], v[176:179], v[90:93]
	v_mfma_f32_16x16x32_f16 v[86:89], v[212:215], v[188:191], v[86:89]
	v_mfma_f32_16x16x32_f16 v[82:85], v[220:223], v[188:191], v[82:85]
	v_mfma_f32_16x16x32_f16 v[78:81], v[212:215], v[196:199], v[78:81]
	v_mfma_f32_16x16x32_f16 v[74:77], v[220:223], v[196:199], v[74:77]
	v_mfma_f32_16x16x32_f16 v[70:73], v[212:215], v[204:207], v[70:73]
	v_mfma_f32_16x16x32_f16 v[66:69], v[220:223], v[204:207], v[66:69]
	s_add_u32 s92, s24, s82
	s_addc_u32 s93, s25, 0
	s_mov_b32 m0, s52
	s_barrier
	ds_read_b128 v[172:175], v147 offset:16384
	ds_read_b128 v[176:179], v147 offset:17408
	ds_read_b128 v[184:187], v146 offset:16384
	ds_read_b128 v[188:191], v146 offset:17408
	ds_read_b128 v[192:195], v145 offset:16384
	ds_read_b128 v[196:199], v145 offset:17408
	ds_read_b128 v[200:203], v144 offset:16384
	ds_read_b128 v[204:207], v144 offset:17408
	global_load_lds_dwordx4 v134, s[92:93]
	s_mov_b32 m0, s86
	s_nop 0
	global_load_lds_dwordx4 v136, s[92:93]
	s_barrier
	s_waitcnt lgkmcnt(7)
	v_mfma_f32_16x16x32_f16 v[62:65], v[152:155], v[172:175], v[62:65]
	v_mfma_f32_16x16x32_f16 v[58:61], v[164:167], v[172:175], v[58:61]
	s_waitcnt lgkmcnt(5)
	v_mfma_f32_16x16x32_f16 v[54:57], v[152:155], v[184:187], v[54:57]
	v_mfma_f32_16x16x32_f16 v[50:53], v[164:167], v[184:187], v[50:53]
	s_waitcnt lgkmcnt(3)
	v_mfma_f32_16x16x32_f16 v[46:49], v[152:155], v[192:195], v[46:49]
	v_mfma_f32_16x16x32_f16 v[42:45], v[164:167], v[192:195], v[42:45]
	s_waitcnt lgkmcnt(1)
	v_mfma_f32_16x16x32_f16 v[38:41], v[152:155], v[200:203], v[38:41]
	v_mfma_f32_16x16x32_f16 v[34:37], v[164:167], v[200:203], v[34:37]
	v_mfma_f32_16x16x32_f16 v[62:65], v[156:159], v[176:179], v[62:65]
	v_mfma_f32_16x16x32_f16 v[58:61], v[168:171], v[176:179], v[58:61]
	v_mfma_f32_16x16x32_f16 v[54:57], v[156:159], v[188:191], v[54:57]
	v_mfma_f32_16x16x32_f16 v[50:53], v[168:171], v[188:191], v[50:53]
	v_mfma_f32_16x16x32_f16 v[46:49], v[156:159], v[196:199], v[46:49]
	v_mfma_f32_16x16x32_f16 v[42:45], v[168:171], v[196:199], v[42:45]
	s_waitcnt lgkmcnt(0)
	v_mfma_f32_16x16x32_f16 v[38:41], v[156:159], v[204:207], v[38:41]
	v_mfma_f32_16x16x32_f16 v[34:37], v[168:171], v[204:207], v[34:37]
	s_barrier
	s_add_u32 s94, s10, s82
	s_addc_u32 s95, s11, 0
	s_mov_b32 m0, s87
	s_nop 0
	global_load_lds_dwordx4 v162, s[94:95]
	s_mov_b32 m0, s88
	s_add_u32 s94, s94, 0x40000
	s_addc_u32 s95, s95, 0
	global_load_lds_dwordx4 v162, s[94:95]
	s_waitcnt vmcnt(6)
	s_barrier
	v_mfma_f32_16x16x32_f16 v[30:33], v[208:211], v[172:175], v[30:33]
	v_mfma_f32_16x16x32_f16 v[26:29], v[216:219], v[172:175], v[26:29]
	v_mfma_f32_16x16x32_f16 v[22:25], v[208:211], v[184:187], v[22:25]
	v_mfma_f32_16x16x32_f16 v[18:21], v[216:219], v[184:187], v[18:21]
	v_mfma_f32_16x16x32_f16 v[14:17], v[208:211], v[192:195], v[14:17]
	v_mfma_f32_16x16x32_f16 v[10:13], v[216:219], v[192:195], v[10:13]
	v_mfma_f32_16x16x32_f16 v[6:9], v[208:211], v[200:203], v[6:9]
	v_mfma_f32_16x16x32_f16 v[2:5], v[216:219], v[200:203], v[2:5]
	v_mfma_f32_16x16x32_f16 v[30:33], v[212:215], v[176:179], v[30:33]
	v_mfma_f32_16x16x32_f16 v[26:29], v[220:223], v[176:179], v[26:29]
	v_mfma_f32_16x16x32_f16 v[22:25], v[212:215], v[188:191], v[22:25]
	v_mfma_f32_16x16x32_f16 v[18:21], v[220:223], v[188:191], v[18:21]
	v_mfma_f32_16x16x32_f16 v[14:17], v[212:215], v[196:199], v[14:17]
	v_mfma_f32_16x16x32_f16 v[10:13], v[220:223], v[196:199], v[10:13]
	v_mfma_f32_16x16x32_f16 v[6:9], v[212:215], v[204:207], v[6:9]
	v_mfma_f32_16x16x32_f16 v[2:5], v[220:223], v[204:207], v[2:5]
	s_barrier
	ds_read_b128 v[152:155], v149
	ds_read_b128 v[156:159], v149 offset:1024
	ds_read_b128 v[164:167], v149 offset:2048
	ds_read_b128 v[168:171], v149 offset:3072
	s_mov_b32 m0, s89
	ds_read_b128 v[172:175], v147 offset:32768
	ds_read_b128 v[176:179], v147 offset:33792
	ds_read_b128 v[184:187], v146 offset:32768
	ds_read_b128 v[188:191], v146 offset:33792
	ds_read_b128 v[192:195], v145 offset:32768
	ds_read_b128 v[196:199], v145 offset:33792
	ds_read_b128 v[200:203], v144 offset:32768
	ds_read_b128 v[204:207], v144 offset:33792
	global_load_lds_dwordx4 v132, s[92:93]
	s_mov_b32 m0, s90
	s_nop 0
	global_load_lds_dwordx4 v130, s[92:93]
	s_waitcnt lgkmcnt(8)
	s_barrier
	s_waitcnt lgkmcnt(7)
	v_mfma_f32_16x16x32_f16 v[126:129], v[152:155], v[172:175], v[126:129]
	v_mfma_f32_16x16x32_f16 v[122:125], v[164:167], v[172:175], v[122:125]
	s_waitcnt lgkmcnt(5)
	v_mfma_f32_16x16x32_f16 v[118:121], v[152:155], v[184:187], v[118:121]
	v_mfma_f32_16x16x32_f16 v[114:117], v[164:167], v[184:187], v[114:117]
	s_waitcnt lgkmcnt(3)
	v_mfma_f32_16x16x32_f16 v[110:113], v[152:155], v[192:195], v[110:113]
	v_mfma_f32_16x16x32_f16 v[106:109], v[164:167], v[192:195], v[106:109]
	s_waitcnt lgkmcnt(1)
	v_mfma_f32_16x16x32_f16 v[102:105], v[152:155], v[200:203], v[102:105]
	v_mfma_f32_16x16x32_f16 v[98:101], v[164:167], v[200:203], v[98:101]
	v_mfma_f32_16x16x32_f16 v[126:129], v[156:159], v[176:179], v[126:129]
	v_mfma_f32_16x16x32_f16 v[122:125], v[168:171], v[176:179], v[122:125]
	v_mfma_f32_16x16x32_f16 v[118:121], v[156:159], v[188:191], v[118:121]
	v_mfma_f32_16x16x32_f16 v[114:117], v[168:171], v[188:191], v[114:117]
	v_mfma_f32_16x16x32_f16 v[110:113], v[156:159], v[196:199], v[110:113]
	v_mfma_f32_16x16x32_f16 v[106:109], v[168:171], v[196:199], v[106:109]
	s_waitcnt lgkmcnt(0)
	v_mfma_f32_16x16x32_f16 v[102:105], v[156:159], v[204:207], v[102:105]
	v_mfma_f32_16x16x32_f16 v[98:101], v[168:171], v[204:207], v[98:101]
	s_barrier
	s_add_u32 s82, s4, s58
	s_addc_u32 s83, s5, 0
	s_add_u32 s92, s82, 0x180
	s_addc_u32 s93, s83, 0
	s_add_i32 m0, s52, 0x18000
	ds_read_b128 v[208:211], v148
	ds_read_b128 v[212:215], v148 offset:1024
	ds_read_b128 v[216:219], v148 offset:2048
	ds_read_b128 v[220:223], v148 offset:3072
	global_load_lds_dwordx4 v162, s[92:93]
	s_add_i32 m0, s52, 0x1a000
	s_add_u32 s92, s92, 0x40000
	s_addc_u32 s93, s93, 0
	global_load_lds_dwordx4 v162, s[92:93]
	s_barrier
	s_waitcnt lgkmcnt(0)
	v_mfma_f32_16x16x32_f16 v[94:97], v[208:211], v[172:175], v[94:97]
	v_mfma_f32_16x16x32_f16 v[90:93], v[216:219], v[172:175], v[90:93]
	v_mfma_f32_16x16x32_f16 v[86:89], v[208:211], v[184:187], v[86:89]
	v_mfma_f32_16x16x32_f16 v[82:85], v[216:219], v[184:187], v[82:85]
	v_mfma_f32_16x16x32_f16 v[78:81], v[208:211], v[192:195], v[78:81]
	v_mfma_f32_16x16x32_f16 v[74:77], v[216:219], v[192:195], v[74:77]
	v_mfma_f32_16x16x32_f16 v[70:73], v[208:211], v[200:203], v[70:73]
	v_mfma_f32_16x16x32_f16 v[66:69], v[216:219], v[200:203], v[66:69]
	v_mfma_f32_16x16x32_f16 v[94:97], v[212:215], v[176:179], v[94:97]
	v_mfma_f32_16x16x32_f16 v[90:93], v[220:223], v[176:179], v[90:93]
	v_mfma_f32_16x16x32_f16 v[86:89], v[212:215], v[188:191], v[86:89]
	v_mfma_f32_16x16x32_f16 v[82:85], v[220:223], v[188:191], v[82:85]
	v_mfma_f32_16x16x32_f16 v[78:81], v[212:215], v[196:199], v[78:81]
	v_mfma_f32_16x16x32_f16 v[74:77], v[220:223], v[196:199], v[74:77]
	v_mfma_f32_16x16x32_f16 v[70:73], v[212:215], v[204:207], v[70:73]
	v_mfma_f32_16x16x32_f16 v[66:69], v[220:223], v[204:207], v[66:69]
	s_add_u32 s92, s59, 0x180
	s_addc_u32 s93, s91, 0
	s_mov_b32 m0, s34
	s_barrier
	ds_read_b128 v[172:175], v147 offset:49152
	ds_read_b128 v[176:179], v147 offset:50176
	ds_read_b128 v[184:187], v146 offset:49152
	ds_read_b128 v[188:191], v146 offset:50176
	ds_read_b128 v[192:195], v145 offset:49152
	ds_read_b128 v[196:199], v145 offset:50176
	ds_read_b128 v[200:203], v144 offset:49152
	ds_read_b128 v[204:207], v144 offset:50176
	global_load_lds_dwordx4 v134, s[92:93]
	s_mov_b32 m0, s35
	s_nop 0
	global_load_lds_dwordx4 v136, s[92:93]
	s_barrier
	s_waitcnt lgkmcnt(7)
	v_mfma_f32_16x16x32_f16 v[62:65], v[152:155], v[172:175], v[62:65]
	v_mfma_f32_16x16x32_f16 v[58:61], v[164:167], v[172:175], v[58:61]
	s_waitcnt lgkmcnt(5)
	v_mfma_f32_16x16x32_f16 v[54:57], v[152:155], v[184:187], v[54:57]
	v_mfma_f32_16x16x32_f16 v[50:53], v[164:167], v[184:187], v[50:53]
	s_waitcnt lgkmcnt(3)
	v_mfma_f32_16x16x32_f16 v[46:49], v[152:155], v[192:195], v[46:49]
	v_mfma_f32_16x16x32_f16 v[42:45], v[164:167], v[192:195], v[42:45]
	s_waitcnt lgkmcnt(1)
	v_mfma_f32_16x16x32_f16 v[38:41], v[152:155], v[200:203], v[38:41]
	v_mfma_f32_16x16x32_f16 v[34:37], v[164:167], v[200:203], v[34:37]
	v_mfma_f32_16x16x32_f16 v[62:65], v[156:159], v[176:179], v[62:65]
	v_mfma_f32_16x16x32_f16 v[58:61], v[168:171], v[176:179], v[58:61]
	v_mfma_f32_16x16x32_f16 v[54:57], v[156:159], v[188:191], v[54:57]
	v_mfma_f32_16x16x32_f16 v[50:53], v[168:171], v[188:191], v[50:53]
	v_mfma_f32_16x16x32_f16 v[46:49], v[156:159], v[196:199], v[46:49]
	v_mfma_f32_16x16x32_f16 v[42:45], v[168:171], v[196:199], v[42:45]
	s_waitcnt lgkmcnt(0)
	v_mfma_f32_16x16x32_f16 v[38:41], v[156:159], v[204:207], v[38:41]
	v_mfma_f32_16x16x32_f16 v[34:37], v[168:171], v[204:207], v[34:37]
	s_barrier
	s_add_u32 s58, s10, s58
	s_addc_u32 s59, s11, 0
	s_add_u32 s58, s58, 0x180
	s_addc_u32 s59, s59, 0
	s_add_i32 m0, s52, 0x1c000
	s_nop 0
	global_load_lds_dwordx4 v162, s[58:59]
	s_add_i32 m0, s52, 0x1e000
	s_add_u32 s58, s58, 0x40000
	s_addc_u32 s59, s59, 0
	global_load_lds_dwordx4 v162, s[58:59]
	s_waitcnt vmcnt(6)
	s_barrier
	v_mfma_f32_16x16x32_f16 v[30:33], v[208:211], v[172:175], v[30:33]
	v_mfma_f32_16x16x32_f16 v[26:29], v[216:219], v[172:175], v[26:29]
	v_mfma_f32_16x16x32_f16 v[22:25], v[208:211], v[184:187], v[22:25]
	v_mfma_f32_16x16x32_f16 v[18:21], v[216:219], v[184:187], v[18:21]
	v_mfma_f32_16x16x32_f16 v[14:17], v[208:211], v[192:195], v[14:17]
	v_mfma_f32_16x16x32_f16 v[10:13], v[216:219], v[192:195], v[10:13]
	v_mfma_f32_16x16x32_f16 v[6:9], v[208:211], v[200:203], v[6:9]
	v_mfma_f32_16x16x32_f16 v[2:5], v[216:219], v[200:203], v[2:5]
	v_mfma_f32_16x16x32_f16 v[30:33], v[212:215], v[176:179], v[30:33]
	v_mfma_f32_16x16x32_f16 v[26:29], v[220:223], v[176:179], v[26:29]
	v_mfma_f32_16x16x32_f16 v[22:25], v[212:215], v[188:191], v[22:25]
	v_mfma_f32_16x16x32_f16 v[18:21], v[220:223], v[188:191], v[18:21]
	v_mfma_f32_16x16x32_f16 v[14:17], v[212:215], v[196:199], v[14:17]
	v_mfma_f32_16x16x32_f16 v[10:13], v[220:223], v[196:199], v[10:13]
	v_mfma_f32_16x16x32_f16 v[6:9], v[212:215], v[204:207], v[6:9]
	v_mfma_f32_16x16x32_f16 v[2:5], v[220:223], v[204:207], v[2:5]
	s_cmp_lt_u32 s84, 28
	s_mov_b32 s84, s57
	s_barrier
	s_cbranch_scc1 .LBB2_382
	v_readlane_b32 s4, v244, 8
	v_readlane_b32 s5, v244, 9
	s_mov_b32 m0, s56
	ds_read_b128 v[134:137], v151
	ds_read_b128 v[152:155], v151 offset:1024
	ds_read_b128 v[156:159], v151 offset:2048
	ds_read_b128 v[164:167], v151 offset:3072
	ds_read_b128 v[168:171], v147
	ds_read_b128 v[172:175], v147 offset:1024
	ds_read_b128 v[176:179], v146
	ds_read_b128 v[184:187], v146 offset:1024
	ds_read_b128 v[188:191], v145
	ds_read_b128 v[192:195], v145 offset:1024
	ds_read_b128 v[196:199], v144
	ds_read_b128 v[200:203], v144 offset:1024
	v_lshl_add_u64 v[132:133], s[4:5], 0, v[132:133]
	global_load_lds_dwordx4 v[132:133], off
	v_lshl_add_u64 v[130:131], s[4:5], 0, v[130:131]
	s_mov_b32 m0, s33
	s_nop 0
	global_load_lds_dwordx4 v[130:131], off
	s_barrier
	s_waitcnt lgkmcnt(0)
	v_mfma_f32_16x16x32_f16 v[126:129], v[134:137], v[168:171], v[126:129]
	v_mfma_f32_16x16x32_f16 v[122:125], v[156:159], v[168:171], v[122:125]
	v_mfma_f32_16x16x32_f16 v[110:113], v[134:137], v[188:191], v[110:113]
	v_mfma_f32_16x16x32_f16 v[106:109], v[156:159], v[188:191], v[106:109]
	v_mfma_f32_16x16x32_f16 v[126:129], v[152:155], v[172:175], v[126:129]
	v_mfma_f32_16x16x32_f16 v[122:125], v[164:167], v[172:175], v[122:125]
	v_mfma_f32_16x16x32_f16 v[118:121], v[134:137], v[176:179], v[118:121]
	v_mfma_f32_16x16x32_f16 v[114:117], v[156:159], v[176:179], v[114:117]
	v_mfma_f32_16x16x32_f16 v[110:113], v[152:155], v[192:195], v[110:113]
	v_mfma_f32_16x16x32_f16 v[106:109], v[164:167], v[192:195], v[106:109]
	v_mfma_f32_16x16x32_f16 v[102:105], v[134:137], v[196:199], v[102:105]
	v_mfma_f32_16x16x32_f16 v[98:101], v[156:159], v[196:199], v[98:101]
	v_mfma_f32_16x16x32_f16 v[130:133], v[152:155], v[184:187], v[118:121]
	v_mfma_f32_16x16x32_f16 v[204:207], v[164:167], v[184:187], v[114:117]
	v_mfma_f32_16x16x32_f16 v[208:211], v[152:155], v[200:203], v[102:105]
	v_mfma_f32_16x16x32_f16 v[212:215], v[164:167], v[200:203], v[98:101]
	s_barrier
	s_nop 1
	ds_read_b128 v[98:101], v150
	ds_read_b128 v[102:105], v150 offset:1024
	ds_read_b128 v[114:117], v150 offset:2048
	ds_read_b128 v[118:121], v150 offset:3072
	s_barrier
	s_waitcnt lgkmcnt(0)
	v_mfma_f32_16x16x32_f16 v[94:97], v[98:101], v[168:171], v[94:97]
	v_mfma_f32_16x16x32_f16 v[90:93], v[114:117], v[168:171], v[90:93]
	v_mfma_f32_16x16x32_f16 v[78:81], v[98:101], v[188:191], v[78:81]
	v_mfma_f32_16x16x32_f16 v[74:77], v[114:117], v[188:191], v[74:77]
	v_mfma_f32_16x16x32_f16 v[94:97], v[102:105], v[172:175], v[94:97]
	v_mfma_f32_16x16x32_f16 v[90:93], v[118:121], v[172:175], v[90:93]
	v_mfma_f32_16x16x32_f16 v[86:89], v[98:101], v[176:179], v[86:89]
	v_mfma_f32_16x16x32_f16 v[82:85], v[114:117], v[176:179], v[82:85]
	v_mfma_f32_16x16x32_f16 v[78:81], v[102:105], v[192:195], v[78:81]
	v_mfma_f32_16x16x32_f16 v[74:77], v[118:121], v[192:195], v[74:77]
	v_mfma_f32_16x16x32_f16 v[70:73], v[98:101], v[196:199], v[70:73]
	v_mfma_f32_16x16x32_f16 v[66:69], v[114:117], v[196:199], v[66:69]
	v_mfma_f32_16x16x32_f16 v[168:171], v[102:105], v[184:187], v[86:89]
	v_mfma_f32_16x16x32_f16 v[172:175], v[118:121], v[184:187], v[82:85]
	v_mfma_f32_16x16x32_f16 v[176:179], v[102:105], v[200:203], v[70:73]
	v_mfma_f32_16x16x32_f16 v[184:187], v[118:121], v[200:203], v[66:69]
	s_barrier
	s_nop 1
	ds_read_b128 v[66:69], v147 offset:16384
	ds_read_b128 v[70:73], v147 offset:17408
	ds_read_b128 v[82:85], v146 offset:16384
	ds_read_b128 v[86:89], v146 offset:17408
	ds_read_b128 v[188:191], v145 offset:16384
	ds_read_b128 v[192:195], v145 offset:17408
	ds_read_b128 v[196:199], v144 offset:16384
	ds_read_b128 v[200:203], v144 offset:17408
	s_waitcnt vmcnt(4)
	s_barrier
	s_waitcnt lgkmcnt(0)
	v_mfma_f32_16x16x32_f16 v[62:65], v[134:137], v[66:69], v[62:65]
	v_mfma_f32_16x16x32_f16 v[58:61], v[156:159], v[66:69], v[58:61]
	v_mfma_f32_16x16x32_f16 v[46:49], v[134:137], v[188:191], v[46:49]
	v_mfma_f32_16x16x32_f16 v[42:45], v[156:159], v[188:191], v[42:45]
	v_mfma_f32_16x16x32_f16 v[62:65], v[152:155], v[70:73], v[62:65]
	v_mfma_f32_16x16x32_f16 v[58:61], v[164:167], v[70:73], v[58:61]
	v_mfma_f32_16x16x32_f16 v[54:57], v[134:137], v[82:85], v[54:57]
	v_mfma_f32_16x16x32_f16 v[50:53], v[156:159], v[82:85], v[50:53]
	v_mfma_f32_16x16x32_f16 v[46:49], v[152:155], v[192:195], v[46:49]
	v_mfma_f32_16x16x32_f16 v[42:45], v[164:167], v[192:195], v[42:45]
	v_mfma_f32_16x16x32_f16 v[38:41], v[134:137], v[196:199], v[38:41]
	v_mfma_f32_16x16x32_f16 v[34:37], v[156:159], v[196:199], v[34:37]
	v_mfma_f32_16x16x32_f16 v[216:219], v[152:155], v[86:89], v[54:57]
	v_mfma_f32_16x16x32_f16 v[220:223], v[164:167], v[86:89], v[50:53]
	v_mfma_f32_16x16x32_f16 v[134:137], v[152:155], v[200:203], v[38:41]
	v_mfma_f32_16x16x32_f16 v[150:153], v[164:167], v[200:203], v[34:37]
	v_mfma_f32_16x16x32_f16 v[30:33], v[98:101], v[66:69], v[30:33]
	v_mfma_f32_16x16x32_f16 v[26:29], v[114:117], v[66:69], v[26:29]
	v_mfma_f32_16x16x32_f16 v[14:17], v[98:101], v[188:191], v[14:17]
	v_mfma_f32_16x16x32_f16 v[10:13], v[114:117], v[188:191], v[10:13]
	v_mfma_f32_16x16x32_f16 v[30:33], v[102:105], v[70:73], v[30:33]
	v_mfma_f32_16x16x32_f16 v[26:29], v[118:121], v[70:73], v[26:29]
	v_mfma_f32_16x16x32_f16 v[22:25], v[98:101], v[82:85], v[22:25]
	v_mfma_f32_16x16x32_f16 v[18:21], v[114:117], v[82:85], v[18:21]
	v_mfma_f32_16x16x32_f16 v[14:17], v[102:105], v[192:195], v[14:17]
	v_mfma_f32_16x16x32_f16 v[10:13], v[118:121], v[192:195], v[10:13]
	v_mfma_f32_16x16x32_f16 v[6:9], v[98:101], v[196:199], v[6:9]
	v_mfma_f32_16x16x32_f16 v[2:5], v[114:117], v[196:199], v[2:5]
	v_mfma_f32_16x16x32_f16 v[154:157], v[102:105], v[86:89], v[22:25]
	v_mfma_f32_16x16x32_f16 v[158:161], v[118:121], v[86:89], v[18:21]
	v_mfma_f32_16x16x32_f16 v[164:167], v[102:105], v[200:203], v[6:9]
	v_mfma_f32_16x16x32_f16 v[188:191], v[118:121], v[200:203], v[2:5]
	s_barrier
	s_nop 1
	ds_read_b128 v[2:5], v149
	ds_read_b128 v[6:9], v149 offset:1024
	ds_read_b128 v[192:195], v149 offset:2048
	ds_read_b128 v[196:199], v149 offset:3072
	ds_read_b128 v[18:21], v147 offset:32768
	ds_read_b128 v[22:25], v147 offset:33792
	ds_read_b128 v[34:37], v146 offset:32768
	ds_read_b128 v[38:41], v146 offset:33792
	ds_read_b128 v[50:53], v145 offset:32768
	ds_read_b128 v[54:57], v145 offset:33792
	ds_read_b128 v[200:203], v144 offset:32768
	ds_read_b128 v[224:227], v144 offset:33792
	s_waitcnt vmcnt(2)
	s_barrier
	s_waitcnt lgkmcnt(0)
	v_mfma_f32_16x16x32_f16 v[66:69], v[2:5], v[18:21], v[126:129]
	v_mfma_f32_16x16x32_f16 v[118:121], v[6:9], v[22:25], v[66:69]
	v_mfma_f32_16x16x32_f16 v[66:69], v[192:195], v[18:21], v[122:125]
	v_mfma_f32_16x16x32_f16 v[114:117], v[196:199], v[22:25], v[66:69]
	v_mfma_f32_16x16x32_f16 v[66:69], v[2:5], v[34:37], v[130:133]
	v_mfma_f32_16x16x32_f16 v[102:105], v[6:9], v[38:41], v[66:69]
	v_mfma_f32_16x16x32_f16 v[66:69], v[192:195], v[34:37], v[204:207]
	v_mfma_f32_16x16x32_f16 v[98:101], v[196:199], v[38:41], v[66:69]
	v_mfma_f32_16x16x32_f16 v[66:69], v[2:5], v[50:53], v[110:113]
	v_mfma_f32_16x16x32_f16 v[86:89], v[6:9], v[54:57], v[66:69]
	v_mfma_f32_16x16x32_f16 v[66:69], v[192:195], v[50:53], v[106:109]
	v_mfma_f32_16x16x32_f16 v[82:85], v[196:199], v[54:57], v[66:69]
	v_mfma_f32_16x16x32_f16 v[66:69], v[2:5], v[200:203], v[208:211]
	v_mfma_f32_16x16x32_f16 v[70:73], v[6:9], v[224:227], v[66:69]
	v_mfma_f32_16x16x32_f16 v[66:69], v[192:195], v[200:203], v[212:215]
	v_mfma_f32_16x16x32_f16 v[66:69], v[196:199], v[224:227], v[66:69]
	s_barrier
	ds_read_b128 v[130:133], v148
	ds_read_b128 v[204:207], v148 offset:1024
	ds_read_b128 v[208:211], v148 offset:2048
	ds_read_b128 v[212:215], v148 offset:3072
	s_waitcnt vmcnt(0)
	s_barrier
	s_waitcnt lgkmcnt(0)
	v_mfma_f32_16x16x32_f16 v[94:97], v[130:133], v[18:21], v[94:97]
	v_mfma_f32_16x16x32_f16 v[18:21], v[208:211], v[18:21], v[90:93]
	v_mfma_f32_16x16x32_f16 v[122:125], v[212:215], v[22:25], v[18:21]
	v_mfma_f32_16x16x32_f16 v[18:21], v[130:133], v[34:37], v[168:171]
	v_mfma_f32_16x16x32_f16 v[110:113], v[204:207], v[38:41], v[18:21]
	v_mfma_f32_16x16x32_f16 v[18:21], v[208:211], v[34:37], v[172:175]
	v_mfma_f32_16x16x32_f16 v[106:109], v[212:215], v[38:41], v[18:21]
	v_mfma_f32_16x16x32_f16 v[18:21], v[130:133], v[50:53], v[78:81]
	v_mfma_f32_16x16x32_f16 v[126:129], v[204:207], v[22:25], v[94:97]
	v_mfma_f32_16x16x32_f16 v[94:97], v[204:207], v[54:57], v[18:21]
	v_mfma_f32_16x16x32_f16 v[18:21], v[208:211], v[50:53], v[74:77]
	v_mfma_f32_16x16x32_f16 v[90:93], v[212:215], v[54:57], v[18:21]
	v_mfma_f32_16x16x32_f16 v[18:21], v[130:133], v[200:203], v[176:179]
	v_mfma_f32_16x16x32_f16 v[78:81], v[204:207], v[224:227], v[18:21]
	v_mfma_f32_16x16x32_f16 v[18:21], v[208:211], v[200:203], v[184:187]
	v_mfma_f32_16x16x32_f16 v[74:77], v[212:215], v[224:227], v[18:21]
	s_barrier
	ds_read_b128 v[168:171], v147 offset:49152
	ds_read_b128 v[172:175], v147 offset:50176
	ds_read_b128 v[176:179], v146 offset:49152
	ds_read_b128 v[146:149], v146 offset:50176
	ds_read_b128 v[184:187], v145 offset:49152
	ds_read_b128 v[200:203], v145 offset:50176
	ds_read_b128 v[224:227], v144 offset:49152
	ds_read_b128 v[228:231], v144 offset:50176
	s_barrier
	s_waitcnt lgkmcnt(0)
	v_mfma_f32_16x16x32_f16 v[18:21], v[2:5], v[168:171], v[62:65]
	v_mfma_f32_16x16x32_f16 v[54:57], v[6:9], v[172:175], v[18:21]
	v_mfma_f32_16x16x32_f16 v[18:21], v[192:195], v[168:171], v[58:61]
	v_mfma_f32_16x16x32_f16 v[50:53], v[196:199], v[172:175], v[18:21]
	v_mfma_f32_16x16x32_f16 v[18:21], v[2:5], v[176:179], v[216:219]
	v_mfma_f32_16x16x32_f16 v[38:41], v[6:9], v[146:149], v[18:21]
	v_mfma_f32_16x16x32_f16 v[18:21], v[192:195], v[176:179], v[220:223]
	v_mfma_f32_16x16x32_f16 v[34:37], v[196:199], v[146:149], v[18:21]
	v_mfma_f32_16x16x32_f16 v[18:21], v[2:5], v[184:187], v[46:49]
	v_mfma_f32_16x16x32_f16 v[2:5], v[2:5], v[224:227], v[134:137]
	v_mfma_f32_16x16x32_f16 v[22:25], v[6:9], v[200:203], v[18:21]
	v_mfma_f32_16x16x32_f16 v[18:21], v[192:195], v[184:187], v[42:45]
	v_mfma_f32_16x16x32_f16 v[6:9], v[6:9], v[228:231], v[2:5]
	v_mfma_f32_16x16x32_f16 v[2:5], v[192:195], v[224:227], v[150:153]
	v_mfma_f32_16x16x32_f16 v[18:21], v[196:199], v[200:203], v[18:21]
	v_mfma_f32_16x16x32_f16 v[2:5], v[196:199], v[228:231], v[2:5]
	v_mfma_f32_16x16x32_f16 v[26:29], v[208:211], v[168:171], v[26:29]
	v_mfma_f32_16x16x32_f16 v[58:61], v[212:215], v[172:175], v[26:29]
	v_mfma_f32_16x16x32_f16 v[26:29], v[130:133], v[176:179], v[154:157]
	v_mfma_f32_16x16x32_f16 v[46:49], v[204:207], v[146:149], v[26:29]
	v_mfma_f32_16x16x32_f16 v[26:29], v[208:211], v[176:179], v[158:161]
	v_mfma_f32_16x16x32_f16 v[10:13], v[208:211], v[184:187], v[10:13]
	v_mfma_f32_16x16x32_f16 v[30:33], v[130:133], v[168:171], v[30:33]
	v_mfma_f32_16x16x32_f16 v[42:45], v[212:215], v[146:149], v[26:29]
	v_mfma_f32_16x16x32_f16 v[14:17], v[130:133], v[184:187], v[14:17]
	v_mfma_f32_16x16x32_f16 v[26:29], v[212:215], v[200:203], v[10:13]
	v_mfma_f32_16x16x32_f16 v[10:13], v[130:133], v[224:227], v[164:167]
	v_mfma_f32_16x16x32_f16 v[62:65], v[204:207], v[172:175], v[30:33]
	v_mfma_f32_16x16x32_f16 v[30:33], v[204:207], v[200:203], v[14:17]
	v_mfma_f32_16x16x32_f16 v[14:17], v[204:207], v[228:231], v[10:13]
	v_mfma_f32_16x16x32_f16 v[10:13], v[208:211], v[224:227], v[188:191]
	v_mfma_f32_16x16x32_f16 v[10:13], v[212:215], v[228:231], v[10:13]
